# epilogue de-serialisation: rotary cos/sin table loads in the q/k projection epilogue issued four at a time per two row groups instead of one dependent pair per group
# baseline (speedup 1.0000x reference)
; DI unsigned cvt_pk_bf16(float lo, float hi) { const f32x2_t v = {lo, hi}; return __builtin_bit_cast(unsigned, __builtin_convertvector(v, bf16x2_t)); }
;     DI void operator()(const f32x4 (&acc)[2][2][4][2], const Unit& u, int wr, int wc, int fr, int fq) const {
;     ...
;             bf16* base = H5 + (size_t)(t >> 2) * NTOK * 1024 + (t & 3) * 256 + wc * 16 + 4 * fq;
; #pragma unroll
;             for (int ai = 0; ai < 2; ++ai)
; #pragma unroll
;                 for (int m = 0; m < 4; ++m) { const int row = row0 + ai * HALF + m * 16; const int pos = row & (S_ - 1);
;                     const f32x4 c = *(const f32x4*)(cosT + pos * 64 + wc * 16 + 4 * fq) * sc, s = *(const f32x4*)(sinT + pos * 64 + wc * 16 + 4 * fq) * sc;
;                     bf16* rowp = base + (size_t)row * 1024;
; #pragma unroll
;                     for (int bj = 0; bj < 2; ++bj) { const f32x4 x1 = acc[ai][bj][m][0], x2 = acc[ai][bj][m][1];
;                         const f32x4 o1 = x1 * c - x2 * s, o2 = x1 * s + x2 * c;
;                         *(u32x2*)(rowp + bj * HALF) = (u32x2){cvt_pk_bf16(o1[0], o1[1]), cvt_pk_bf16(o1[2], o1[3])};
;                         *(u32x2*)(rowp + bj * HALF + 64) = (u32x2){cvt_pk_bf16(o2[0], o2[1]), cvt_pk_bf16(o2[2], o2[3])}; } }
.Lmy_rot_0_0:
	v_lshlrev_b32_e32 v184, 8, v142
	v_and_b32_e32 v186, 0x7cf00, v184
	v_mov_b32_e32 v187, v131
	v_lshl_add_u64 v[188:189], v[136:137], 0, v[186:187]
	global_load_dwordx4 v[204:207], v[188:189], off
	v_lshl_add_u64 v[188:189], v[138:139], 0, v[186:187]
	global_load_dwordx4 v[200:203], v[188:189], off
	v_lshlrev_b32_e32 v184, 8, v152
	v_and_b32_e32 v186, 0x7df00, v184
	v_mov_b32_e32 v187, v131
	v_lshl_add_u64 v[188:189], v[136:137], 0, v[186:187]
	global_load_dwordx4 v[196:199], v[188:189], off
	v_lshl_add_u64 v[188:189], v[138:139], 0, v[186:187]
	global_load_dwordx4 v[192:195], v[188:189], off
	v_lshlrev_b32_e32 v130, 8, v142
	v_and_b32_e32 v130, 0x7cf00, v130
	v_lshl_add_u64 v[146:147], v[136:137], 0, v[130:131]
	s_nop 0
	v_lshl_add_u64 v[146:147], v[138:139], 0, v[130:131]
	s_nop 0
	s_cmp_lt_i32 s16, 4
	s_cselect_b64 vcc, -1, 0
	s_ashr_i32 s42, s16, 2
	s_ashr_i32 s43, s42, 31
	s_lshl_b64 s[42:43], s[42:43], 24
	s_add_u32 s20, s74, s42
	s_addc_u32 s42, s75, s43
	s_lshl_b32 s43, s16, 9
	s_and_b32 s43, s43, 0x600
	s_add_u32 s20, s20, s43
	v_cndmask_b32_e32 v144, 1.0, v159, vcc
	s_addc_u32 s43, s42, 0
	v_readlane_b32 s42, v254, 3
	s_add_u32 s42, s20, s42
	v_mov_b32_e32 v141, v131
	s_addc_u32 s43, s43, 0
	v_lshlrev_b64 v[168:169], 11, v[142:143]
	v_lshlrev_b32_e32 v130, 8, v152
	v_lshl_add_u64 v[146:147], s[42:43], 0, v[140:141]
	v_and_b32_e32 v130, 0x7df00, v130
	v_lshl_add_u64 v[168:169], v[146:147], 0, v[168:169]
	v_lshl_add_u64 v[170:171], v[136:137], 0, v[130:131]
	v_lshlrev_b64 v[152:153], 11, v[152:153]
	v_lshl_add_u64 v[152:153], v[146:147], 0, v[152:153]
	s_nop 0
	s_waitcnt vmcnt(3)
	v_pk_mul_f32 v[160:161], v[144:145], v[204:205] op_sel_hi:[0,1]
	v_pk_mul_f32 v[162:163], v[144:145], v[206:207] op_sel_hi:[0,1]
	s_nop 0
	s_waitcnt vmcnt(2)
	v_pk_mul_f32 v[166:167], v[144:145], v[202:203] op_sel_hi:[0,1]
	v_pk_mul_f32 v[164:165], v[144:145], v[200:201] op_sel_hi:[0,1]
	v_pk_mul_f32 v[172:173], v[120:121], v[164:165]
	v_pk_mul_f32 v[174:175], v[122:123], v[166:167]
	v_pk_mul_f32 v[176:177], v[124:125], v[164:165]
	v_pk_mul_f32 v[178:179], v[126:127], v[166:167]
	v_pk_mul_f32 v[180:181], v[88:89], v[164:165]
	v_pk_mul_f32 v[182:183], v[90:91], v[166:167]
	v_pk_mul_f32 v[164:165], v[92:93], v[164:165]
	v_pk_mul_f32 v[166:167], v[94:95], v[166:167]
	v_pk_fma_f32 v[174:175], v[126:127], v[162:163], v[174:175] neg_lo:[0,0,1] neg_hi:[0,0,1]
	v_pk_fma_f32 v[172:173], v[124:125], v[160:161], v[172:173] neg_lo:[0,0,1] neg_hi:[0,0,1]
	v_pk_fma_f32 v[178:179], v[122:123], v[162:163], v[178:179]
	v_pk_fma_f32 v[176:177], v[120:121], v[160:161], v[176:177]
	v_pk_fma_f32 v[182:183], v[94:95], v[162:163], v[182:183] neg_lo:[0,0,1] neg_hi:[0,0,1]
	v_pk_fma_f32 v[180:181], v[92:93], v[160:161], v[180:181] neg_lo:[0,0,1] neg_hi:[0,0,1]
	v_pk_fma_f32 v[162:163], v[90:91], v[162:163], v[166:167]
	v_pk_fma_f32 v[160:161], v[88:89], v[160:161], v[164:165]
	v_cvt_pk_bf16_f32 v164, v172, v173
	v_cvt_pk_bf16_f32 v165, v174, v175
	v_cvt_pk_bf16_f32 v166, v176, v177
	v_cvt_pk_bf16_f32 v167, v178, v179
	v_cvt_pk_bf16_f32 v172, v180, v181
	v_cvt_pk_bf16_f32 v173, v182, v183
	v_cvt_pk_bf16_f32 v160, v160, v161
	v_cvt_pk_bf16_f32 v161, v162, v163
	global_store_dwordx2 v[168:169], v[164:165], off
	global_store_dwordx2 v[168:169], v[166:167], off offset:128
	global_store_dwordx2 v[168:169], v[172:173], off offset:256
	global_store_dwordx2 v[168:169], v[160:161], off offset:384
	v_lshl_add_u64 v[164:165], v[138:139], 0, v[130:131]
	s_nop 0
	v_lshlrev_b32_e32 v130, 8, v150
	s_nop 0
	v_and_b32_e32 v130, 0x7ef00, v130
	v_lshl_add_u64 v[168:169], v[136:137], 0, v[130:131]
	v_lshlrev_b64 v[150:151], 11, v[150:151]
	v_lshl_add_u64 v[150:151], v[146:147], 0, v[150:151]
	s_nop 0
	s_waitcnt vmcnt(5)
	v_pk_mul_f32 v[160:161], v[144:145], v[196:197] op_sel_hi:[0,1]
	v_pk_mul_f32 v[162:163], v[144:145], v[198:199] op_sel_hi:[0,1]
	s_nop 0
	s_waitcnt vmcnt(4)
	v_pk_mul_f32 v[166:167], v[144:145], v[194:195] op_sel_hi:[0,1]
	v_pk_mul_f32 v[164:165], v[144:145], v[192:193] op_sel_hi:[0,1]
	v_pk_mul_f32 v[170:171], v[112:113], v[164:165]
	v_pk_mul_f32 v[172:173], v[114:115], v[166:167]
	v_pk_mul_f32 v[174:175], v[116:117], v[164:165]
	v_pk_mul_f32 v[176:177], v[118:119], v[166:167]
	v_pk_mul_f32 v[178:179], v[80:81], v[164:165]
	v_pk_mul_f32 v[180:181], v[82:83], v[166:167]
	v_pk_mul_f32 v[164:165], v[84:85], v[164:165]
	v_pk_mul_f32 v[166:167], v[86:87], v[166:167]
	v_pk_fma_f32 v[172:173], v[118:119], v[162:163], v[172:173] neg_lo:[0,0,1] neg_hi:[0,0,1]
	v_pk_fma_f32 v[170:171], v[116:117], v[160:161], v[170:171] neg_lo:[0,0,1] neg_hi:[0,0,1]
	v_pk_fma_f32 v[176:177], v[114:115], v[162:163], v[176:177]
	v_pk_fma_f32 v[174:175], v[112:113], v[160:161], v[174:175]
	v_pk_fma_f32 v[180:181], v[86:87], v[162:163], v[180:181] neg_lo:[0,0,1] neg_hi:[0,0,1]
	v_pk_fma_f32 v[178:179], v[84:85], v[160:161], v[178:179] neg_lo:[0,0,1] neg_hi:[0,0,1]
	v_pk_fma_f32 v[162:163], v[82:83], v[162:163], v[166:167]
	v_pk_fma_f32 v[160:161], v[80:81], v[160:161], v[164:165]
	v_cvt_pk_bf16_f32 v164, v170, v171
	v_cvt_pk_bf16_f32 v165, v172, v173
	v_cvt_pk_bf16_f32 v166, v174, v175
	v_cvt_pk_bf16_f32 v167, v176, v177
	v_cvt_pk_bf16_f32 v170, v178, v179
	v_cvt_pk_bf16_f32 v171, v180, v181
	v_cvt_pk_bf16_f32 v160, v160, v161
	v_cvt_pk_bf16_f32 v161, v162, v163
	global_store_dwordx2 v[152:153], v[164:165], off
	global_store_dwordx2 v[152:153], v[166:167], off offset:128
	global_store_dwordx2 v[152:153], v[170:171], off offset:256
	global_store_dwordx2 v[152:153], v[160:161], off offset:384
; DI unsigned cvt_pk_bf16(float lo, float hi) { const f32x2_t v = {lo, hi}; return __builtin_bit_cast(unsigned, __builtin_convertvector(v, bf16x2_t)); }
;     DI void operator()(const f32x4 (&acc)[2][2][4][2], const Unit& u, int wr, int wc, int fr, int fq) const {
;     ...
;             bf16* base = H5 + (size_t)(t >> 2) * NTOK * 1024 + (t & 3) * 256 + wc * 16 + 4 * fq;
; #pragma unroll
;             for (int ai = 0; ai < 2; ++ai)
; #pragma unroll
;                 for (int m = 0; m < 4; ++m) { const int row = row0 + ai * HALF + m * 16; const int pos = row & (S_ - 1);
;                     const f32x4 c = *(const f32x4*)(cosT + pos * 64 + wc * 16 + 4 * fq) * sc, s = *(const f32x4*)(sinT + pos * 64 + wc * 16 + 4 * fq) * sc;
;                     bf16* rowp = base + (size_t)row * 1024;
; #pragma unroll
;                     for (int bj = 0; bj < 2; ++bj) { const f32x4 x1 = acc[ai][bj][m][0], x2 = acc[ai][bj][m][1];
;                         const f32x4 o1 = x1 * c - x2 * s, o2 = x1 * s + x2 * c;
;                         *(u32x2*)(rowp + bj * HALF) = (u32x2){cvt_pk_bf16(o1[0], o1[1]), cvt_pk_bf16(o1[2], o1[3])};
;                         *(u32x2*)(rowp + bj * HALF + 64) = (u32x2){cvt_pk_bf16(o2[0], o2[1]), cvt_pk_bf16(o2[2], o2[3])}; } }
.Lmy_rot_0_1:
	global_load_dwordx4 v[204:207], v[168:169], off
	v_lshl_add_u64 v[180:181], v[138:139], 0, v[130:131]
	global_load_dwordx4 v[200:203], v[180:181], off
	v_lshlrev_b32_e32 v180, 8, v148
	v_and_b32_e32 v182, 0x7ff00, v180
	v_mov_b32_e32 v183, v131
	v_lshl_add_u64 v[184:185], v[136:137], 0, v[182:183]
	global_load_dwordx4 v[196:199], v[184:185], off
	v_lshl_add_u64 v[184:185], v[138:139], 0, v[182:183]
	global_load_dwordx4 v[192:195], v[184:185], off
	v_lshl_add_u64 v[152:153], v[138:139], 0, v[130:131]
	s_nop 0
	s_nop 0
	v_lshlrev_b32_e32 v130, 8, v148
	v_and_b32_e32 v130, 0x7ff00, v130
	v_lshl_add_u64 v[152:153], v[136:137], 0, v[130:131]
	v_lshlrev_b64 v[148:149], 11, v[148:149]
	v_lshl_add_u64 v[148:149], v[146:147], 0, v[148:149]
	s_nop 0
	s_waitcnt vmcnt(3)
	v_pk_mul_f32 v[160:161], v[144:145], v[204:205] op_sel_hi:[0,1]
	s_nop 0
	s_waitcnt vmcnt(2)
	v_pk_mul_f32 v[166:167], v[144:145], v[202:203] op_sel_hi:[0,1]
	v_pk_mul_f32 v[164:165], v[144:145], v[200:201] op_sel_hi:[0,1]
	v_pk_mul_f32 v[162:163], v[144:145], v[206:207] op_sel_hi:[0,1]
	v_pk_mul_f32 v[168:169], v[104:105], v[164:165]
	v_pk_mul_f32 v[170:171], v[106:107], v[166:167]
	v_pk_mul_f32 v[172:173], v[108:109], v[164:165]
	v_pk_mul_f32 v[174:175], v[110:111], v[166:167]
	v_pk_mul_f32 v[176:177], v[72:73], v[164:165]
	v_pk_mul_f32 v[178:179], v[74:75], v[166:167]
	v_pk_mul_f32 v[164:165], v[76:77], v[164:165]
	v_pk_mul_f32 v[166:167], v[78:79], v[166:167]
	v_pk_fma_f32 v[170:171], v[110:111], v[162:163], v[170:171] neg_lo:[0,0,1] neg_hi:[0,0,1]
	v_pk_fma_f32 v[168:169], v[108:109], v[160:161], v[168:169] neg_lo:[0,0,1] neg_hi:[0,0,1]
	v_pk_fma_f32 v[174:175], v[106:107], v[162:163], v[174:175]
	v_pk_fma_f32 v[172:173], v[104:105], v[160:161], v[172:173]
	v_pk_fma_f32 v[178:179], v[78:79], v[162:163], v[178:179] neg_lo:[0,0,1] neg_hi:[0,0,1]
	v_pk_fma_f32 v[176:177], v[76:77], v[160:161], v[176:177] neg_lo:[0,0,1] neg_hi:[0,0,1]
	v_pk_fma_f32 v[162:163], v[74:75], v[162:163], v[166:167]
	v_pk_fma_f32 v[160:161], v[72:73], v[160:161], v[164:165]
	v_cvt_pk_bf16_f32 v164, v168, v169
	v_cvt_pk_bf16_f32 v165, v170, v171
	v_cvt_pk_bf16_f32 v166, v172, v173
	v_cvt_pk_bf16_f32 v167, v174, v175
	v_cvt_pk_bf16_f32 v168, v176, v177
	v_cvt_pk_bf16_f32 v169, v178, v179
	v_cvt_pk_bf16_f32 v160, v160, v161
	v_cvt_pk_bf16_f32 v161, v162, v163
	global_store_dwordx2 v[150:151], v[164:165], off
	global_store_dwordx2 v[150:151], v[166:167], off offset:128
	global_store_dwordx2 v[150:151], v[168:169], off offset:256
	global_store_dwordx2 v[150:151], v[160:161], off offset:384
	v_lshl_add_u64 v[150:151], v[138:139], 0, v[130:131]
	s_nop 0
	s_nop 0
	v_add_u32_e32 v150, 0x80, v142
	v_lshlrev_b32_e32 v130, 8, v150
	v_and_b32_e32 v130, 0x7cf00, v130
	v_lshl_add_u64 v[152:153], v[136:137], 0, v[130:131]
	v_ashrrev_i32_e32 v151, 31, v150
	v_lshlrev_b64 v[150:151], 11, v[150:151]
	v_lshl_add_u64 v[150:151], v[146:147], 0, v[150:151]
	s_nop 0
	s_waitcnt vmcnt(5)
	v_pk_mul_f32 v[160:161], v[144:145], v[196:197] op_sel_hi:[0,1]
	s_nop 0
	s_waitcnt vmcnt(4)
	v_pk_mul_f32 v[166:167], v[144:145], v[194:195] op_sel_hi:[0,1]
	v_pk_mul_f32 v[164:165], v[144:145], v[192:193] op_sel_hi:[0,1]
	v_pk_mul_f32 v[162:163], v[144:145], v[198:199] op_sel_hi:[0,1]
	v_pk_mul_f32 v[168:169], v[96:97], v[164:165]
	v_pk_mul_f32 v[170:171], v[98:99], v[166:167]
	v_pk_mul_f32 v[172:173], v[100:101], v[164:165]
	v_pk_mul_f32 v[174:175], v[102:103], v[166:167]
	v_pk_mul_f32 v[176:177], v[64:65], v[164:165]
	v_pk_mul_f32 v[178:179], v[66:67], v[166:167]
	v_pk_mul_f32 v[164:165], v[68:69], v[164:165]
	v_pk_mul_f32 v[166:167], v[70:71], v[166:167]
	v_pk_fma_f32 v[170:171], v[102:103], v[162:163], v[170:171] neg_lo:[0,0,1] neg_hi:[0,0,1]
	v_pk_fma_f32 v[168:169], v[100:101], v[160:161], v[168:169] neg_lo:[0,0,1] neg_hi:[0,0,1]
	v_pk_fma_f32 v[174:175], v[98:99], v[162:163], v[174:175]
	v_pk_fma_f32 v[172:173], v[96:97], v[160:161], v[172:173]
	v_pk_fma_f32 v[178:179], v[70:71], v[162:163], v[178:179] neg_lo:[0,0,1] neg_hi:[0,0,1]
	v_pk_fma_f32 v[176:177], v[68:69], v[160:161], v[176:177] neg_lo:[0,0,1] neg_hi:[0,0,1]
	v_pk_fma_f32 v[162:163], v[66:67], v[162:163], v[166:167]
	v_pk_fma_f32 v[160:161], v[64:65], v[160:161], v[164:165]
	v_cvt_pk_bf16_f32 v164, v168, v169
	v_cvt_pk_bf16_f32 v165, v170, v171
	v_cvt_pk_bf16_f32 v166, v172, v173
	v_cvt_pk_bf16_f32 v167, v174, v175
	v_cvt_pk_bf16_f32 v168, v176, v177
	v_cvt_pk_bf16_f32 v169, v178, v179
	v_cvt_pk_bf16_f32 v160, v160, v161
	v_cvt_pk_bf16_f32 v161, v162, v163
	global_store_dwordx2 v[148:149], v[164:165], off
	global_store_dwordx2 v[148:149], v[166:167], off offset:128
	global_store_dwordx2 v[148:149], v[168:169], off offset:256
	global_store_dwordx2 v[148:149], v[160:161], off offset:384
; DI unsigned cvt_pk_bf16(float lo, float hi) { const f32x2_t v = {lo, hi}; return __builtin_bit_cast(unsigned, __builtin_convertvector(v, bf16x2_t)); }
;     DI void operator()(const f32x4 (&acc)[2][2][4][2], const Unit& u, int wr, int wc, int fr, int fq) const {
;     ...
;             bf16* base = H5 + (size_t)(t >> 2) * NTOK * 1024 + (t & 3) * 256 + wc * 16 + 4 * fq;
; #pragma unroll
;             for (int ai = 0; ai < 2; ++ai)
; #pragma unroll
;                 for (int m = 0; m < 4; ++m) { const int row = row0 + ai * HALF + m * 16; const int pos = row & (S_ - 1);
;                     const f32x4 c = *(const f32x4*)(cosT + pos * 64 + wc * 16 + 4 * fq) * sc, s = *(const f32x4*)(sinT + pos * 64 + wc * 16 + 4 * fq) * sc;
;                     bf16* rowp = base + (size_t)row * 1024;
; #pragma unroll
;                     for (int bj = 0; bj < 2; ++bj) { const f32x4 x1 = acc[ai][bj][m][0], x2 = acc[ai][bj][m][1];
;                         const f32x4 o1 = x1 * c - x2 * s, o2 = x1 * s + x2 * c;
;                         *(u32x2*)(rowp + bj * HALF) = (u32x2){cvt_pk_bf16(o1[0], o1[1]), cvt_pk_bf16(o1[2], o1[3])};
;                         *(u32x2*)(rowp + bj * HALF + 64) = (u32x2){cvt_pk_bf16(o2[0], o2[1]), cvt_pk_bf16(o2[2], o2[3])}; } }
.Lmy_rot_0_2:
	global_load_dwordx4 v[204:207], v[152:153], off
	v_lshl_add_u64 v[180:181], v[138:139], 0, v[130:131]
	global_load_dwordx4 v[200:203], v[180:181], off
	v_add_u32_e32 v180, 0x90, v142
	v_lshlrev_b32_e32 v182, 8, v180
	v_and_b32_e32 v184, 0x7df00, v182
	v_mov_b32_e32 v185, v131
	v_lshl_add_u64 v[186:187], v[136:137], 0, v[184:185]
	global_load_dwordx4 v[196:199], v[186:187], off
	v_lshl_add_u64 v[186:187], v[138:139], 0, v[184:185]
	global_load_dwordx4 v[192:195], v[186:187], off
	v_lshl_add_u64 v[148:149], v[138:139], 0, v[130:131]
	s_nop 0
	s_nop 0
	v_add_u32_e32 v148, 0x90, v142
	v_lshlrev_b32_e32 v130, 8, v148
	v_and_b32_e32 v130, 0x7df00, v130
	v_lshl_add_u64 v[152:153], v[136:137], 0, v[130:131]
	v_ashrrev_i32_e32 v149, 31, v148
	v_lshlrev_b64 v[148:149], 11, v[148:149]
	v_lshl_add_u64 v[148:149], v[146:147], 0, v[148:149]
	s_nop 0
	s_waitcnt vmcnt(3)
	v_pk_mul_f32 v[160:161], v[144:145], v[204:205] op_sel_hi:[0,1]
	s_nop 0
	s_waitcnt vmcnt(2)
	v_pk_mul_f32 v[166:167], v[144:145], v[202:203] op_sel_hi:[0,1]
	v_pk_mul_f32 v[164:165], v[144:145], v[200:201] op_sel_hi:[0,1]
	v_pk_mul_f32 v[162:163], v[144:145], v[206:207] op_sel_hi:[0,1]
	v_pk_mul_f32 v[168:169], v[56:57], v[164:165]
	v_pk_mul_f32 v[170:171], v[58:59], v[166:167]
	v_pk_mul_f32 v[172:173], v[60:61], v[164:165]
	v_pk_mul_f32 v[174:175], v[62:63], v[166:167]
	v_pk_mul_f32 v[176:177], v[24:25], v[164:165]
	v_pk_mul_f32 v[178:179], v[26:27], v[166:167]
	v_pk_mul_f32 v[164:165], v[28:29], v[164:165]
	v_pk_mul_f32 v[166:167], v[30:31], v[166:167]
	v_pk_fma_f32 v[170:171], v[62:63], v[162:163], v[170:171] neg_lo:[0,0,1] neg_hi:[0,0,1]
	v_pk_fma_f32 v[168:169], v[60:61], v[160:161], v[168:169] neg_lo:[0,0,1] neg_hi:[0,0,1]
	v_pk_fma_f32 v[174:175], v[58:59], v[162:163], v[174:175]
	v_pk_fma_f32 v[172:173], v[56:57], v[160:161], v[172:173]
	v_pk_fma_f32 v[178:179], v[30:31], v[162:163], v[178:179] neg_lo:[0,0,1] neg_hi:[0,0,1]
	v_pk_fma_f32 v[176:177], v[28:29], v[160:161], v[176:177] neg_lo:[0,0,1] neg_hi:[0,0,1]
	v_pk_fma_f32 v[162:163], v[26:27], v[162:163], v[166:167]
	v_pk_fma_f32 v[160:161], v[24:25], v[160:161], v[164:165]
	v_cvt_pk_bf16_f32 v164, v168, v169
	v_cvt_pk_bf16_f32 v165, v170, v171
	v_cvt_pk_bf16_f32 v166, v172, v173
	v_cvt_pk_bf16_f32 v167, v174, v175
	v_cvt_pk_bf16_f32 v168, v176, v177
	v_cvt_pk_bf16_f32 v169, v178, v179
	v_cvt_pk_bf16_f32 v160, v160, v161
	v_cvt_pk_bf16_f32 v161, v162, v163
	global_store_dwordx2 v[150:151], v[164:165], off
	global_store_dwordx2 v[150:151], v[166:167], off offset:128
	global_store_dwordx2 v[150:151], v[168:169], off offset:256
	global_store_dwordx2 v[150:151], v[160:161], off offset:384
	v_lshl_add_u64 v[150:151], v[138:139], 0, v[130:131]
	s_nop 0
	s_nop 0
	v_add_u32_e32 v150, 0xa0, v142
	v_lshlrev_b32_e32 v130, 8, v150
	v_and_b32_e32 v130, 0x7ef00, v130
	v_lshl_add_u64 v[152:153], v[136:137], 0, v[130:131]
	v_add_u32_e32 v142, 0xb0, v142
	v_ashrrev_i32_e32 v151, 31, v150
	v_ashrrev_i32_e32 v143, 31, v142
	s_nop 0
	s_waitcnt vmcnt(5)
	v_pk_mul_f32 v[160:161], v[144:145], v[196:197] op_sel_hi:[0,1]
	s_nop 0
	s_waitcnt vmcnt(4)
	v_pk_mul_f32 v[166:167], v[144:145], v[194:195] op_sel_hi:[0,1]
	v_pk_mul_f32 v[164:165], v[144:145], v[192:193] op_sel_hi:[0,1]
	v_pk_mul_f32 v[162:163], v[144:145], v[198:199] op_sel_hi:[0,1]
	v_pk_mul_f32 v[168:169], v[48:49], v[164:165]
	v_pk_mul_f32 v[170:171], v[50:51], v[166:167]
	v_pk_mul_f32 v[172:173], v[52:53], v[164:165]
	v_pk_mul_f32 v[174:175], v[54:55], v[166:167]
	v_pk_mul_f32 v[176:177], v[16:17], v[164:165]
	v_pk_mul_f32 v[178:179], v[18:19], v[166:167]
	v_pk_mul_f32 v[164:165], v[20:21], v[164:165]
	v_pk_mul_f32 v[166:167], v[22:23], v[166:167]
	v_pk_fma_f32 v[170:171], v[54:55], v[162:163], v[170:171] neg_lo:[0,0,1] neg_hi:[0,0,1]
	v_pk_fma_f32 v[168:169], v[52:53], v[160:161], v[168:169] neg_lo:[0,0,1] neg_hi:[0,0,1]
	v_pk_fma_f32 v[174:175], v[50:51], v[162:163], v[174:175]
	v_pk_fma_f32 v[172:173], v[48:49], v[160:161], v[172:173]
	v_pk_fma_f32 v[178:179], v[22:23], v[162:163], v[178:179] neg_lo:[0,0,1] neg_hi:[0,0,1]
	v_pk_fma_f32 v[176:177], v[20:21], v[160:161], v[176:177] neg_lo:[0,0,1] neg_hi:[0,0,1]
	v_pk_fma_f32 v[162:163], v[18:19], v[162:163], v[166:167]
	v_pk_fma_f32 v[160:161], v[16:17], v[160:161], v[164:165]
	v_cvt_pk_bf16_f32 v164, v168, v169
	v_cvt_pk_bf16_f32 v165, v170, v171
	v_cvt_pk_bf16_f32 v166, v172, v173
	v_cvt_pk_bf16_f32 v167, v174, v175
	v_cvt_pk_bf16_f32 v168, v176, v177
	v_cvt_pk_bf16_f32 v169, v178, v179
	v_cvt_pk_bf16_f32 v160, v160, v161
	v_cvt_pk_bf16_f32 v161, v162, v163
	global_store_dwordx2 v[148:149], v[164:165], off
	global_store_dwordx2 v[148:149], v[166:167], off offset:128
	global_store_dwordx2 v[148:149], v[168:169], off offset:256
	global_store_dwordx2 v[148:149], v[160:161], off offset:384
; DI unsigned cvt_pk_bf16(float lo, float hi) { const f32x2_t v = {lo, hi}; return __builtin_bit_cast(unsigned, __builtin_convertvector(v, bf16x2_t)); }
;     DI void operator()(const f32x4 (&acc)[2][2][4][2], const Unit& u, int wr, int wc, int fr, int fq) const {
;     ...
;             bf16* base = H5 + (size_t)(t >> 2) * NTOK * 1024 + (t & 3) * 256 + wc * 16 + 4 * fq;
; #pragma unroll
;             for (int ai = 0; ai < 2; ++ai)
; #pragma unroll
;                 for (int m = 0; m < 4; ++m) { const int row = row0 + ai * HALF + m * 16; const int pos = row & (S_ - 1);
;                     const f32x4 c = *(const f32x4*)(cosT + pos * 64 + wc * 16 + 4 * fq) * sc, s = *(const f32x4*)(sinT + pos * 64 + wc * 16 + 4 * fq) * sc;
;                     bf16* rowp = base + (size_t)row * 1024;
; #pragma unroll
;                     for (int bj = 0; bj < 2; ++bj) { const f32x4 x1 = acc[ai][bj][m][0], x2 = acc[ai][bj][m][1];
;                         const f32x4 o1 = x1 * c - x2 * s, o2 = x1 * s + x2 * c;
;                         *(u32x2*)(rowp + bj * HALF) = (u32x2){cvt_pk_bf16(o1[0], o1[1]), cvt_pk_bf16(o1[2], o1[3])};
;                         *(u32x2*)(rowp + bj * HALF + 64) = (u32x2){cvt_pk_bf16(o2[0], o2[1]), cvt_pk_bf16(o2[2], o2[3])}; } }
.Lmy_rot_0_3:
	global_load_dwordx4 v[204:207], v[152:153], off
	v_lshl_add_u64 v[178:179], v[138:139], 0, v[130:131]
	global_load_dwordx4 v[200:203], v[178:179], off
	v_lshlrev_b32_e32 v178, 8, v142
	v_and_b32_e32 v180, 0x7ff00, v178
	v_mov_b32_e32 v181, v131
	v_lshl_add_u64 v[182:183], v[136:137], 0, v[180:181]
	global_load_dwordx4 v[196:199], v[182:183], off
	v_lshl_add_u64 v[182:183], v[138:139], 0, v[180:181]
	global_load_dwordx4 v[192:195], v[182:183], off
	v_lshl_add_u64 v[148:149], v[138:139], 0, v[130:131]
	s_nop 0
	s_nop 0
	v_lshlrev_b32_e32 v130, 8, v142
	v_lshlrev_b64 v[148:149], 11, v[150:151]
	v_and_b32_e32 v130, 0x7ff00, v130
	v_lshl_add_u64 v[148:149], v[146:147], 0, v[148:149]
	v_lshl_add_u64 v[150:151], v[136:137], 0, v[130:131]
	v_lshlrev_b64 v[142:143], 11, v[142:143]
	v_lshl_add_u64 v[142:143], v[146:147], 0, v[142:143]
	s_nop 0
	s_waitcnt vmcnt(3)
	v_pk_mul_f32 v[152:153], v[144:145], v[204:205] op_sel_hi:[0,1]
	v_pk_mul_f32 v[160:161], v[144:145], v[206:207] op_sel_hi:[0,1]
	s_nop 0
	s_waitcnt vmcnt(2)
	v_pk_mul_f32 v[162:163], v[144:145], v[202:203] op_sel_hi:[0,1]
	v_pk_mul_f32 v[164:165], v[144:145], v[200:201] op_sel_hi:[0,1]
	v_pk_mul_f32 v[166:167], v[40:41], v[164:165]
	v_pk_mul_f32 v[168:169], v[42:43], v[162:163]
	v_pk_mul_f32 v[170:171], v[44:45], v[164:165]
	v_pk_mul_f32 v[172:173], v[46:47], v[162:163]
	v_pk_mul_f32 v[174:175], v[8:9], v[164:165]
	v_pk_mul_f32 v[176:177], v[10:11], v[162:163]
	v_pk_mul_f32 v[164:165], v[12:13], v[164:165]
	v_pk_mul_f32 v[162:163], v[14:15], v[162:163]
	v_pk_fma_f32 v[168:169], v[46:47], v[160:161], v[168:169] neg_lo:[0,0,1] neg_hi:[0,0,1]
	v_pk_fma_f32 v[166:167], v[44:45], v[152:153], v[166:167] neg_lo:[0,0,1] neg_hi:[0,0,1]
	v_pk_fma_f32 v[172:173], v[42:43], v[160:161], v[172:173]
	v_pk_fma_f32 v[170:171], v[40:41], v[152:153], v[170:171]
	v_pk_fma_f32 v[176:177], v[14:15], v[160:161], v[176:177] neg_lo:[0,0,1] neg_hi:[0,0,1]
	v_pk_fma_f32 v[174:175], v[12:13], v[152:153], v[174:175] neg_lo:[0,0,1] neg_hi:[0,0,1]
	v_pk_fma_f32 v[160:161], v[10:11], v[160:161], v[162:163]
	v_pk_fma_f32 v[152:153], v[8:9], v[152:153], v[164:165]
	v_cvt_pk_bf16_f32 v162, v166, v167
	v_cvt_pk_bf16_f32 v163, v168, v169
	v_cvt_pk_bf16_f32 v152, v152, v153
	v_cvt_pk_bf16_f32 v153, v160, v161
	v_cvt_pk_bf16_f32 v164, v170, v171
	v_cvt_pk_bf16_f32 v165, v172, v173
	v_cvt_pk_bf16_f32 v166, v174, v175
	v_cvt_pk_bf16_f32 v167, v176, v177
	global_store_dwordx2 v[148:149], v[162:163], off
	global_store_dwordx2 v[148:149], v[164:165], off offset:128
	global_store_dwordx2 v[148:149], v[166:167], off offset:256
	global_store_dwordx2 v[148:149], v[152:153], off offset:384
	v_lshl_add_u64 v[152:153], v[138:139], 0, v[130:131]
	s_nop 0
	s_nop 0
	s_nop 0
	s_nop 0
	s_waitcnt vmcnt(5)
	v_pk_mul_f32 v[146:147], v[144:145], v[196:197] op_sel_hi:[0,1]
	v_pk_mul_f32 v[148:149], v[144:145], v[198:199] op_sel_hi:[0,1]
	s_nop 0
	s_waitcnt vmcnt(4)
	v_pk_mul_f32 v[150:151], v[144:145], v[194:195] op_sel_hi:[0,1]
	v_pk_mul_f32 v[152:153], v[144:145], v[192:193] op_sel_hi:[0,1]
	v_pk_mul_f32 v[160:161], v[32:33], v[152:153]
	v_pk_mul_f32 v[162:163], v[34:35], v[150:151]
	v_pk_mul_f32 v[164:165], v[36:37], v[152:153]
	v_pk_mul_f32 v[166:167], v[38:39], v[150:151]
	v_pk_mul_f32 v[168:169], v[0:1], v[152:153]
	v_pk_mul_f32 v[170:171], v[2:3], v[150:151]
	v_pk_mul_f32 v[152:153], v[4:5], v[152:153]
	v_pk_mul_f32 v[150:151], v[6:7], v[150:151]
	v_pk_fma_f32 v[162:163], v[38:39], v[148:149], v[162:163] neg_lo:[0,0,1] neg_hi:[0,0,1]
	v_pk_fma_f32 v[160:161], v[36:37], v[146:147], v[160:161] neg_lo:[0,0,1] neg_hi:[0,0,1]
	v_pk_fma_f32 v[166:167], v[34:35], v[148:149], v[166:167]
	v_pk_fma_f32 v[164:165], v[32:33], v[146:147], v[164:165]
	v_pk_fma_f32 v[170:171], v[6:7], v[148:149], v[170:171] neg_lo:[0,0,1] neg_hi:[0,0,1]
	v_pk_fma_f32 v[168:169], v[4:5], v[146:147], v[168:169] neg_lo:[0,0,1] neg_hi:[0,0,1]
	v_pk_fma_f32 v[148:149], v[2:3], v[148:149], v[150:151]
	v_pk_fma_f32 v[146:147], v[0:1], v[146:147], v[152:153]
	v_cvt_pk_bf16_f32 v150, v160, v161
	v_cvt_pk_bf16_f32 v151, v162, v163
	v_cvt_pk_bf16_f32 v152, v164, v165
	v_cvt_pk_bf16_f32 v153, v166, v167
	v_cvt_pk_bf16_f32 v160, v168, v169
	v_cvt_pk_bf16_f32 v161, v170, v171
	v_cvt_pk_bf16_f32 v146, v146, v147
	v_cvt_pk_bf16_f32 v147, v148, v149
	global_store_dwordx2 v[142:143], v[150:151], off
	global_store_dwordx2 v[142:143], v[152:153], off offset:128
	global_store_dwordx2 v[142:143], v[160:161], off offset:256
	global_store_dwordx2 v[142:143], v[146:147], off offset:384
